# DPP reductions also in attention epilogue and ssm_finish GLU (counted LDS waits after removed shuffles made full waits)
# speedup vs baseline: 1.0058x; 1.0006x over previous
.LBB0_355:
	v_add_u32_e32 v61, s8, v224
	ds_read_b64 v[68:69], v61
	v_pk_mul_f32 v[62:63], v[66:67], v[142:143] op_sel_hi:[1,0]
	v_add_u32_e32 v65, s8, v223
	v_pk_fma_f32 v[70:71], v[124:125], v[140:141], v[62:63] neg_lo:[0,0,1] neg_hi:[0,0,1]
	v_pk_fma_f32 v[62:63], v[124:125], v[140:141], v[62:63] op_sel_hi:[1,0,1]
	s_addk_i32 s8, 0x940
	v_mov_b32_e32 v71, v63
	s_waitcnt lgkmcnt(0)
	v_pk_add_f32 v[62:63], v[70:71], v[68:69]
	s_cmpk_eq_i32 s8, 0x2500
	v_cvt_pk_bf16_f32 v70, v62, v63
	v_pk_mul_f32 v[68:69], v[66:67], v[62:63] op_sel:[0,1]
	ds_write_b32 v65, v70
	v_pk_fma_f32 v[70:71], v[124:125], v[62:63], v[68:69] neg_lo:[0,0,1] neg_hi:[0,0,1]
	v_pk_fma_f32 v[62:63], v[124:125], v[62:63], v[68:69] op_sel_hi:[1,0,1]
	ds_read_b64 v[68:69], v61 offset:592
	v_mov_b32_e32 v71, v63
	s_waitcnt lgkmcnt(0)
	v_pk_add_f32 v[62:63], v[70:71], v[68:69]
	s_nop 0
	v_cvt_pk_bf16_f32 v70, v62, v63
	ds_write_b32 v65, v70 offset:592
	ds_read_b64 v[72:73], v61 offset:1184
	v_pk_mul_f32 v[68:69], v[66:67], v[62:63] op_sel:[0,1]
	s_nop 0
	v_pk_fma_f32 v[70:71], v[124:125], v[62:63], v[68:69] neg_lo:[0,0,1] neg_hi:[0,0,1]
	v_pk_fma_f32 v[62:63], v[124:125], v[62:63], v[68:69] op_sel_hi:[1,0,1]
	s_nop 0
	v_mov_b32_e32 v71, v63
	s_waitcnt lgkmcnt(0)
	v_pk_add_f32 v[62:63], v[70:71], v[72:73]
	s_nop 0
	v_cvt_pk_bf16_f32 v70, v62, v63
	ds_write_b32 v65, v70 offset:1184
	ds_read_b64 v[70:71], v61 offset:1776
	v_pk_mul_f32 v[68:69], v[66:67], v[62:63] op_sel:[0,1]
	s_nop 0
	v_pk_fma_f32 v[72:73], v[124:125], v[62:63], v[68:69] neg_lo:[0,0,1] neg_hi:[0,0,1]
	v_pk_fma_f32 v[62:63], v[124:125], v[62:63], v[68:69] op_sel_hi:[1,0,1]
	s_nop 0
	v_mov_b32_e32 v73, v63
	s_waitcnt lgkmcnt(0)
	v_pk_add_f32 v[140:141], v[72:73], v[70:71]
	s_nop 0
	v_mov_b32_e32 v142, v141
	v_cvt_pk_bf16_f32 v61, v140, v141
	ds_write_b32 v65, v61 offset:1776
	s_cbranch_scc0 .LBB0_355
	ds_read_b128 v[68:71], v60 offset:36864
	ds_read_b128 v[72:75], v60 offset:36928
	v_lshl_or_b32 v65, s10, 4, v163
	s_add_i32 s10, s10, 1
	s_cmp_eq_u32 s10, 4
	s_waitcnt lgkmcnt(1)
	v_mfma_f32_16x16x32_bf16 v[68:71], v[68:71], v[8:11], 0
	s_waitcnt lgkmcnt(0)
	v_mfma_f32_16x16x32_bf16 v[68:71], v[72:75], v[12:15], v[68:71]
	ds_read_b128 v[72:75], v60 offset:36992
	s_waitcnt lgkmcnt(0)
	v_mfma_f32_16x16x32_bf16 v[68:71], v[72:75], v[16:19], v[68:71]
	ds_read_b128 v[72:75], v60 offset:37056
	ds_read_b128 v[60:63], v60 offset:37376
	s_waitcnt lgkmcnt(1)
	v_mfma_f32_16x16x32_bf16 v[68:71], v[72:75], v[20:23], v[68:71]
	s_waitcnt lgkmcnt(0)
	v_mfma_f32_16x16x32_bf16 v[60:63], v[60:63], v[56:59], v[68:71]
	s_nop 7
	v_mul_f32_e32 v68, 0x3d372713, v60
	v_mul_f32_e32 v68, v60, v68
	v_fma_f32 v68, v60, v68, v60
	v_mul_f32_e32 v68, 0x3fcc422a, v68
	v_mul_f32_e32 v68, 0xbfb8aa3b, v68
	v_exp_f32_e32 v68, v68
	s_nop 0
	v_add_f32_e32 v68, 1.0, v68
	v_rcp_f32_e32 v68, v68
	s_nop 0
	v_mul_f32_e32 v60, v60, v68
	v_cvt_pk_bf16_f32 v60, v60, s0
	v_mad_u64_u32 v[68:69], s[8:9], v65, s3, v[64:65]
	ds_write_b16 v68, v60
	v_mul_f32_e32 v60, 0x3d372713, v61
	v_mul_f32_e32 v60, v61, v60
	v_fma_f32 v60, v61, v60, v61
	v_mul_f32_e32 v60, 0x3fcc422a, v60
	v_mul_f32_e32 v60, 0xbfb8aa3b, v60
	v_exp_f32_e32 v60, v60
	s_nop 0
	v_add_f32_e32 v60, 1.0, v60
	v_rcp_f32_e32 v60, v60
	s_nop 0
	v_mul_f32_e32 v60, v61, v60
	v_cvt_pk_bf16_f32 v60, v60, s0
	ds_write_b16 v68, v60 offset:528
	v_mul_f32_e32 v60, 0x3d372713, v62
	v_mul_f32_e32 v60, v62, v60
	v_fma_f32 v60, v62, v60, v62
	v_mul_f32_e32 v60, 0x3fcc422a, v60
	v_mul_f32_e32 v60, 0xbfb8aa3b, v60
	v_exp_f32_e32 v60, v60
	s_nop 0
	v_add_f32_e32 v60, 1.0, v60
	v_rcp_f32_e32 v60, v60
	s_nop 0
	v_mul_f32_e32 v60, v62, v60
	v_cvt_pk_bf16_f32 v60, v60, s0
	ds_write_b16 v68, v60 offset:1056
	v_mul_f32_e32 v60, 0x3d372713, v63
	v_mul_f32_e32 v60, v63, v60
	v_fma_f32 v60, v63, v60, v63
	v_mul_f32_e32 v60, 0x3fcc422a, v60
	v_mul_f32_e32 v60, 0xbfb8aa3b, v60
	v_exp_f32_e32 v60, v60
	s_nop 0
	v_add_f32_e32 v60, 1.0, v60
	v_rcp_f32_e32 v60, v60
	s_nop 0
	v_mul_f32_e32 v60, v63, v60
	v_cvt_pk_bf16_f32 v60, v60, s0
	ds_write_b16 v68, v60 offset:1584
	s_cbranch_scc0 .LBB0_352
	s_mov_b32 s8, 8
	s_mov_b64 s[24:25], 0
	s_and_b64 vcc, exec, s[6:7]
	s_cbranch_vccz .LBB0_346
	s_waitcnt lgkmcnt(0)
	s_barrier
	global_load_dword v129, v[112:113], off
	global_load_dword v128, v[114:115], off offset:3072
	global_load_dwordx4 v[76:79], v[116:117], off
	global_load_dwordx4 v[72:75], v[116:117], off offset:32
	global_load_dwordx4 v[68:71], v[116:117], off offset:64
	global_load_dwordx4 v[64:67], v[116:117], off offset:96
	global_load_dwordx4 v[60:63], v[116:117], off offset:128
	global_load_dwordx4 v[56:59], v[116:117], off offset:160
	global_load_dwordx4 v[52:55], v[116:117], off offset:192
	global_load_dwordx4 v[48:51], v[116:117], off offset:224
	global_load_dwordx4 v[44:47], v[116:117], off offset:256
	global_load_dwordx4 v[40:43], v[116:117], off offset:288
	global_load_dwordx4 v[36:39], v[116:117], off offset:320
	global_load_dwordx4 v[32:35], v[116:117], off offset:352
	global_load_dwordx4 v[28:31], v[116:117], off offset:384
	global_load_dwordx4 v[24:27], v[116:117], off offset:416
	global_load_dwordx4 v[20:23], v[116:117], off offset:448
	global_load_dwordx4 v[16:19], v[116:117], off offset:480
	s_waitcnt vmcnt(19)
	ds_read_b128 v[0:3], v229
	ds_read_b128 v[80:83], v229 offset:32
	ds_read_b128 v[84:87], v229 offset:64
	ds_read_b128 v[88:91], v229 offset:96
	s_nop 15
	s_nop 15
	s_waitcnt vmcnt(15) lgkmcnt(3)
	v_mfma_f32_32x32x16_bf16 v[0:15], v[0:3], v[76:79], 0
	s_waitcnt vmcnt(14) lgkmcnt(2)
	v_mfma_f32_32x32x16_bf16 v[0:15], v[80:83], v[72:75], v[0:15]
	s_waitcnt vmcnt(13) lgkmcnt(1)
	v_mfma_f32_32x32x16_bf16 v[0:15], v[84:87], v[68:71], v[0:15]
	s_waitcnt vmcnt(12) lgkmcnt(0)
	v_mfma_f32_32x32x16_bf16 v[0:15], v[88:91], v[64:67], v[0:15]
	s_nop 15
	s_nop 15
	ds_read_b128 v[80:83], v229 offset:128
	ds_read_b128 v[84:87], v229 offset:160
	ds_read_b128 v[88:91], v229 offset:192
	ds_read_b128 v[92:95], v229 offset:224
	s_nop 15
	s_nop 15
	s_waitcnt vmcnt(11) lgkmcnt(3)
	v_mfma_f32_32x32x16_bf16 v[0:15], v[80:83], v[60:63], v[0:15]
	s_waitcnt vmcnt(10) lgkmcnt(2)
	v_mfma_f32_32x32x16_bf16 v[0:15], v[84:87], v[56:59], v[0:15]
	s_waitcnt vmcnt(9) lgkmcnt(1)
	v_mfma_f32_32x32x16_bf16 v[0:15], v[88:91], v[52:55], v[0:15]
	s_waitcnt vmcnt(8) lgkmcnt(0)
	v_mfma_f32_32x32x16_bf16 v[0:15], v[92:95], v[48:51], v[0:15]
	s_nop 15
	s_nop 15
	ds_read_b128 v[80:83], v229 offset:256
	ds_read_b128 v[84:87], v229 offset:288
	ds_read_b128 v[88:91], v229 offset:320
	ds_read_b128 v[92:95], v229 offset:352
	s_nop 15
	s_nop 15
	s_waitcnt vmcnt(7) lgkmcnt(3)
	v_mfma_f32_32x32x16_bf16 v[0:15], v[80:83], v[44:47], v[0:15]
	s_waitcnt vmcnt(6) lgkmcnt(2)
	v_mfma_f32_32x32x16_bf16 v[0:15], v[84:87], v[40:43], v[0:15]
	s_waitcnt vmcnt(5) lgkmcnt(1)
	v_mfma_f32_32x32x16_bf16 v[0:15], v[88:91], v[36:39], v[0:15]
	s_waitcnt vmcnt(4) lgkmcnt(0)
	v_mfma_f32_32x32x16_bf16 v[0:15], v[92:95], v[32:35], v[0:15]
	s_nop 15
	s_nop 15
	ds_read_b128 v[80:83], v229 offset:384
	ds_read_b128 v[84:87], v229 offset:416
	ds_read_b128 v[88:91], v229 offset:448
	ds_read_b128 v[92:95], v229 offset:480
	s_nop 15
	s_nop 15
	s_waitcnt vmcnt(3) lgkmcnt(3)
	v_mfma_f32_32x32x16_bf16 v[0:15], v[80:83], v[28:31], v[0:15]
	s_waitcnt vmcnt(2) lgkmcnt(2)
	v_mfma_f32_32x32x16_bf16 v[0:15], v[84:87], v[24:27], v[0:15]
	s_waitcnt vmcnt(1) lgkmcnt(1)
	v_mfma_f32_32x32x16_bf16 v[0:15], v[88:91], v[20:23], v[0:15]
	s_waitcnt vmcnt(0) lgkmcnt(0)
	v_mfma_f32_32x32x16_bf16 v[0:15], v[92:95], v[16:19], v[0:15]
	s_nop 15
	s_nop 15
	s_nop 11
	v_add_f32_e32 v0, v129, v0
	v_add_f32_e32 v1, v129, v1
	v_mul_f32_e32 v0, 0xbfb8aa3b, v0
	v_mul_f32_e32 v1, 0xbfb8aa3b, v1
	v_exp_f32_e32 v0, v0
	v_exp_f32_e32 v1, v1
	ds_read_u16 v80, v230
	ds_read_u16 v81, v227
	ds_read_u16 v84, v227 offset:528
	ds_read_u16 v85, v227 offset:1056
	ds_read_u16 v88, v227 offset:3696
	ds_read_u16 v89, v227 offset:4224
	ds_read_u16 v92, v227 offset:4752
	ds_read_u16 v93, v227 offset:5280
	s_waitcnt lgkmcnt(6)
	v_lshlrev_b32_e32 v81, 16, v81
	v_add_f32_e32 v0, 1.0, v0
	v_add_f32_e32 v1, 1.0, v1
	v_rcp_f32_e32 v0, v0
	v_rcp_f32_e32 v1, v1
	v_lshlrev_b32_e32 v80, 16, v80
	v_add_f32_e32 v2, v129, v2
	v_mul_f32_e32 v2, 0xbfb8aa3b, v2
	v_pk_mul_f32 v[80:81], v[0:1], v[80:81]
	s_waitcnt lgkmcnt(4)
	v_lshlrev_b32_e32 v85, 16, v85
	v_pk_mul_f32 v[0:1], v[80:81], v[80:81]
	ds_bpermute_b32 v0, v185, v0
	ds_bpermute_b32 v1, v185, v1
	v_lshlrev_b32_e32 v84, 16, v84
	v_add_f32_e32 v6, v129, v6
	v_mul_f32_e32 v6, 0xbfb8aa3b, v6
	s_waitcnt lgkmcnt(4)
	v_lshlrev_b32_e32 v89, 16, v89
	s_waitcnt lgkmcnt(0)
	v_pk_fma_f32 v[0:1], v[80:81], v[80:81], v[0:1]
	s_nop 1
	v_mov_b32_dpp v82, v0 row_ror:8 row_mask:0xf bank_mask:0xf
	s_nop 0
	v_mov_b32_dpp v83, v1 row_ror:8 row_mask:0xf bank_mask:0xf
	v_lshlrev_b32_e32 v88, 16, v88
	v_lshlrev_b32_e32 v93, 16, v93
	v_lshlrev_b32_e32 v92, 16, v92
	v_add_f32_e32 v8, v129, v8
	s_waitcnt lgkmcnt(0)
	v_pk_add_f32 v[0:1], v[0:1], v[82:83]
	v_exp_f32_e32 v82, v2
	v_add_f32_e32 v2, v129, v3
	v_mul_f32_e32 v2, 0xbfb8aa3b, v2
	v_exp_f32_e32 v3, v2
	v_add_f32_e32 v82, 1.0, v82
	v_mov_b32_dpp v2, v0 row_half_mirror row_mask:0xf bank_mask:0xf
	s_nop 1
	v_mov_b32_dpp v2, v2 quad_perm:[3,2,1,0] row_mask:0xf bank_mask:0xf
	v_rcp_f32_e32 v82, v82
	v_add_f32_e32 v3, 1.0, v3
	v_rcp_f32_e32 v83, v3
	s_nop 0
	v_mov_b32_dpp v3, v1 row_half_mirror row_mask:0xf bank_mask:0xf
	s_nop 1
	v_mov_b32_dpp v3, v3 quad_perm:[3,2,1,0] row_mask:0xf bank_mask:0xf
	v_add_f32_e32 v9, v129, v9
	v_mul_f32_e32 v8, 0xbfb8aa3b, v8
	v_pk_mul_f32 v[82:83], v[82:83], v[84:85]
	v_mul_f32_e32 v9, 0xbfb8aa3b, v9
	v_pk_mul_f32 v[84:85], v[82:83], v[82:83]
	s_waitcnt lgkmcnt(0)
	v_pk_add_f32 v[0:1], v[0:1], v[2:3]
	ds_bpermute_b32 v84, v185, v84
	ds_bpermute_b32 v85, v185, v85
	v_mov_b32_dpp v2, v0 quad_perm:[2,3,0,1] row_mask:0xf bank_mask:0xf
	v_mov_b32_dpp v3, v1 quad_perm:[2,3,0,1] row_mask:0xf bank_mask:0xf
	v_exp_f32_e32 v8, v8
	v_exp_f32_e32 v9, v9
	s_waitcnt lgkmcnt(0)
	v_pk_fma_f32 v[84:85], v[82:83], v[82:83], v[84:85]
	s_nop 1
	v_mov_b32_dpp v86, v84 row_ror:8 row_mask:0xf bank_mask:0xf
	s_waitcnt lgkmcnt(0)
	v_pk_add_f32 v[0:1], v[0:1], v[2:3]
	v_add_f32_e32 v3, v129, v4
	v_mov_b32_dpp v87, v85 row_ror:8 row_mask:0xf bank_mask:0xf
	v_mul_f32_e32 v3, 0xbfb8aa3b, v3
	v_add_f32_e32 v4, v129, v5
	v_exp_f32_e32 v3, v3
	v_mul_f32_e32 v4, 0xbfb8aa3b, v4
	v_exp_f32_e32 v5, v4
	s_waitcnt lgkmcnt(0)
	v_pk_add_f32 v[86:87], v[84:85], v[86:87]
	v_add_f32_e32 v3, 1.0, v3
	s_nop 0
	v_mov_b32_dpp v4, v86 row_half_mirror row_mask:0xf bank_mask:0xf
	s_nop 1
	v_mov_b32_dpp v4, v4 quad_perm:[3,2,1,0] row_mask:0xf bank_mask:0xf
	v_rcp_f32_e32 v84, v3
	v_add_f32_e32 v3, 1.0, v5
	v_mov_b32_dpp v5, v87 row_half_mirror row_mask:0xf bank_mask:0xf
	s_nop 1
	v_mov_b32_dpp v5, v5 quad_perm:[3,2,1,0] row_mask:0xf bank_mask:0xf
	v_rcp_f32_e32 v85, v3
	v_add_f32_e32 v8, 1.0, v8
	v_add_f32_e32 v9, 1.0, v9
	v_rcp_f32_e32 v8, v8
	s_waitcnt lgkmcnt(0)
	v_pk_add_f32 v[4:5], v[86:87], v[4:5]
	v_exp_f32_e32 v86, v6
	v_add_f32_e32 v6, v129, v7
	v_mul_f32_e32 v6, 0xbfb8aa3b, v6
	v_pk_mul_f32 v[84:85], v[84:85], v[88:89]
	v_exp_f32_e32 v7, v6
	v_pk_mul_f32 v[88:89], v[84:85], v[84:85]
	ds_bpermute_b32 v88, v185, v88
	ds_bpermute_b32 v89, v185, v89
	v_add_f32_e32 v86, 1.0, v86
	v_add_f32_e32 v7, 1.0, v7
	v_rcp_f32_e32 v86, v86
	v_rcp_f32_e32 v87, v7
	s_waitcnt lgkmcnt(0)
	v_pk_fma_f32 v[88:89], v[84:85], v[84:85], v[88:89]
	s_nop 1
	v_mov_b32_dpp v6, v88 row_ror:8 row_mask:0xf bank_mask:0xf
	s_nop 0
	v_mov_b32_dpp v7, v89 row_ror:8 row_mask:0xf bank_mask:0xf
	v_mov_b32_dpp v90, v4 quad_perm:[2,3,0,1] row_mask:0xf bank_mask:0xf
	v_mov_b32_dpp v91, v5 quad_perm:[2,3,0,1] row_mask:0xf bank_mask:0xf
	v_pk_mul_f32 v[86:87], v[86:87], v[92:93]
	v_rcp_f32_e32 v9, v9
	v_pk_mul_f32 v[92:93], v[86:87], v[86:87]
	ds_bpermute_b32 v92, v185, v92
	ds_bpermute_b32 v93, v185, v93
	s_waitcnt lgkmcnt(0)
	v_pk_add_f32 v[88:89], v[88:89], v[6:7]
	s_waitcnt lgkmcnt(0)
	v_pk_add_f32 v[4:5], v[4:5], v[90:91]
	v_mov_b32_dpp v90, v88 row_half_mirror row_mask:0xf bank_mask:0xf
	s_nop 1
	v_mov_b32_dpp v90, v90 quad_perm:[3,2,1,0] row_mask:0xf bank_mask:0xf
	v_mov_b32_dpp v91, v89 row_half_mirror row_mask:0xf bank_mask:0xf
	s_nop 1
	v_mov_b32_dpp v91, v91 quad_perm:[3,2,1,0] row_mask:0xf bank_mask:0xf
	s_waitcnt lgkmcnt(0)
	v_pk_fma_f32 v[92:93], v[86:87], v[86:87], v[92:93]
	s_nop 1
	v_mov_b32_dpp v94, v92 row_ror:8 row_mask:0xf bank_mask:0xf
	s_nop 0
	v_mov_b32_dpp v95, v93 row_ror:8 row_mask:0xf bank_mask:0xf
	v_add_f32_e32 v10, v129, v10
	s_waitcnt lgkmcnt(0)
	v_pk_add_f32 v[90:91], v[88:89], v[90:91]
	ds_read_u16 v88, v227 offset:7920
	ds_read_u16 v89, v227 offset:8448
	ds_read_u16 v120, v227 offset:8976
	ds_read_u16 v121, v227 offset:9504
	ds_read_u16 v124, v227 offset:12144
	ds_read_u16 v125, v227 offset:12672
	ds_read_u16 v126, v227 offset:13200
	ds_read_u16 v127, v227 offset:13728
	s_waitcnt lgkmcnt(0)
	v_lshlrev_b32_e32 v89, 16, v89
	v_lshlrev_b32_e32 v88, 16, v88
	v_pk_mul_f32 v[88:89], v[8:9], v[88:89]
	v_pk_add_f32 v[92:93], v[92:93], v[94:95]
	v_pk_mul_f32 v[8:9], v[88:89], v[88:89]
	v_add_f32_e32 v11, v129, v11
	v_mov_b32_dpp v94, v92 row_half_mirror row_mask:0xf bank_mask:0xf
	s_nop 1
	v_mov_b32_dpp v94, v94 quad_perm:[3,2,1,0] row_mask:0xf bank_mask:0xf
	v_mov_b32_dpp v95, v93 row_half_mirror row_mask:0xf bank_mask:0xf
	s_nop 1
	v_mov_b32_dpp v95, v95 quad_perm:[3,2,1,0] row_mask:0xf bank_mask:0xf
	ds_bpermute_b32 v8, v185, v8
	ds_bpermute_b32 v9, v185, v9
	v_mul_f32_e32 v10, 0xbfb8aa3b, v10
	v_mul_f32_e32 v11, 0xbfb8aa3b, v11
	v_exp_f32_e32 v10, v10
	v_exp_f32_e32 v11, v11
	v_mov_b32_dpp v96, v90 quad_perm:[2,3,0,1] row_mask:0xf bank_mask:0xf
	v_mov_b32_dpp v97, v91 quad_perm:[2,3,0,1] row_mask:0xf bank_mask:0xf
	s_waitcnt lgkmcnt(0)
	v_pk_add_f32 v[92:93], v[92:93], v[94:95]
	s_waitcnt lgkmcnt(0)
	v_pk_fma_f32 v[100:101], v[88:89], v[88:89], v[8:9]
	v_add_f32_e32 v10, 1.0, v10
	v_add_f32_e32 v11, 1.0, v11
	v_mov_b32_dpp v94, v92 quad_perm:[2,3,0,1] row_mask:0xf bank_mask:0xf
	v_mov_b32_dpp v95, v93 quad_perm:[2,3,0,1] row_mask:0xf bank_mask:0xf
	v_mov_b32_dpp v102, v100 row_ror:8 row_mask:0xf bank_mask:0xf
	v_mov_b32_dpp v103, v101 row_ror:8 row_mask:0xf bank_mask:0xf
	v_rcp_f32_e32 v10, v10
	v_rcp_f32_e32 v11, v11
	s_waitcnt lgkmcnt(0)
	v_pk_add_f32 v[8:9], v[90:91], v[96:97]
	v_lshlrev_b32_e32 v91, 16, v121
	v_lshlrev_b32_e32 v90, 16, v120
	v_pk_mul_f32 v[90:91], v[10:11], v[90:91]
	s_waitcnt lgkmcnt(0)
	v_pk_add_f32 v[98:99], v[92:93], v[94:95]
	s_waitcnt lgkmcnt(0)
	v_pk_add_f32 v[92:93], v[100:101], v[102:103]
	v_pk_mul_f32 v[10:11], v[90:91], v[90:91]
	s_nop 0
	v_mov_b32_dpp v94, v92 row_half_mirror row_mask:0xf bank_mask:0xf
	s_nop 1
	v_mov_b32_dpp v94, v94 quad_perm:[3,2,1,0] row_mask:0xf bank_mask:0xf
	v_mov_b32_dpp v95, v93 row_half_mirror row_mask:0xf bank_mask:0xf
	s_nop 1
	v_mov_b32_dpp v95, v95 quad_perm:[3,2,1,0] row_mask:0xf bank_mask:0xf
	ds_bpermute_b32 v100, v185, v10
	ds_bpermute_b32 v101, v185, v11
	v_add_f32_e32 v12, v129, v12
	v_mul_f32_e32 v12, 0xbfb8aa3b, v12
	s_waitcnt lgkmcnt(0)
	v_pk_add_f32 v[92:93], v[92:93], v[94:95]
	s_nop 1
	v_mov_b32_dpp v94, v92 quad_perm:[2,3,0,1] row_mask:0xf bank_mask:0xf
	s_waitcnt lgkmcnt(0)
	v_pk_fma_f32 v[120:121], v[90:91], v[90:91], v[100:101]
	v_mov_b32_dpp v95, v93 quad_perm:[2,3,0,1] row_mask:0xf bank_mask:0xf
	s_nop 0
	v_mov_b32_dpp v122, v120 row_ror:8 row_mask:0xf bank_mask:0xf
	v_mov_b32_dpp v123, v121 row_ror:8 row_mask:0xf bank_mask:0xf
	v_add_f32_e32 v14, v129, v14
	v_mul_f32_e32 v14, 0xbfb8aa3b, v14
	s_waitcnt lgkmcnt(0)
	v_pk_add_f32 v[100:101], v[92:93], v[94:95]
	v_mov_b32_dpp v2, v0 quad_perm:[1,0,3,2] row_mask:0xf bank_mask:0xf
	s_waitcnt lgkmcnt(0)
	v_pk_add_f32 v[92:93], v[120:121], v[122:123]
	v_exp_f32_e32 v120, v12
	v_add_f32_e32 v12, v129, v13
	v_mov_b32_dpp v94, v92 row_half_mirror row_mask:0xf bank_mask:0xf
	s_nop 1
	v_mov_b32_dpp v94, v94 quad_perm:[3,2,1,0] row_mask:0xf bank_mask:0xf
	v_mov_b32_dpp v95, v93 row_half_mirror row_mask:0xf bank_mask:0xf
	s_nop 1
	v_mov_b32_dpp v95, v95 quad_perm:[3,2,1,0] row_mask:0xf bank_mask:0xf
	v_mul_f32_e32 v12, 0xbfb8aa3b, v12
	v_exp_f32_e32 v121, v12
	v_mov_b32_dpp v3, v1 quad_perm:[1,0,3,2] row_mask:0xf bank_mask:0xf
	v_mov_b32_dpp v6, v4 quad_perm:[1,0,3,2] row_mask:0xf bank_mask:0xf
	s_waitcnt lgkmcnt(0)
	v_pk_add_f32 v[12:13], v[92:93], v[94:95]
	v_add_f32_e32 v92, 1.0, v120
	v_add_f32_e32 v93, 1.0, v121
	v_rcp_f32_e32 v92, v92
	v_rcp_f32_e32 v93, v93
	v_exp_f32_e32 v121, v14
	v_add_f32_e32 v14, v129, v15
	v_mul_f32_e32 v14, 0xbfb8aa3b, v14
	v_exp_f32_e32 v15, v14
	v_lshlrev_b32_e32 v95, 16, v125
	v_lshlrev_b32_e32 v94, 16, v124
	v_pk_mul_f32 v[92:93], v[92:93], v[94:95]
	v_add_f32_e32 v15, 1.0, v15
	v_pk_mul_f32 v[94:95], v[92:93], v[92:93]
	ds_bpermute_b32 v14, v185, v94
	v_add_f32_e32 v94, 1.0, v121
	v_rcp_f32_e32 v122, v94
	v_rcp_f32_e32 v123, v15
	ds_bpermute_b32 v15, v185, v95
	v_lshlrev_b32_e32 v95, 16, v127
	v_lshlrev_b32_e32 v94, 16, v126
	v_pk_mul_f32 v[94:95], v[122:123], v[94:95]
	v_mov_b32_dpp v120, v12 quad_perm:[2,3,0,1] row_mask:0xf bank_mask:0xf
	v_pk_mul_f32 v[122:123], v[94:95], v[94:95]
	ds_bpermute_b32 v122, v185, v122
	ds_bpermute_b32 v123, v185, v123
	s_waitcnt lgkmcnt(0)
	v_pk_fma_f32 v[14:15], v[92:93], v[92:93], v[14:15]
	v_mov_b32_dpp v121, v13 quad_perm:[2,3,0,1] row_mask:0xf bank_mask:0xf
	s_nop 0
	v_mov_b32_dpp v124, v14 row_ror:8 row_mask:0xf bank_mask:0xf
	v_mov_b32_dpp v125, v15 row_ror:8 row_mask:0xf bank_mask:0xf
	s_waitcnt lgkmcnt(0)
	v_pk_fma_f32 v[122:123], v[94:95], v[94:95], v[122:123]
	s_nop 1
	v_mov_b32_dpp v126, v122 row_ror:8 row_mask:0xf bank_mask:0xf
	s_nop 0
	v_mov_b32_dpp v127, v123 row_ror:8 row_mask:0xf bank_mask:0xf
	s_waitcnt lgkmcnt(0)
	v_pk_add_f32 v[12:13], v[12:13], v[120:121]
	s_waitcnt lgkmcnt(0)
	v_pk_add_f32 v[120:121], v[14:15], v[124:125]
	s_nop 1
	v_mov_b32_dpp v124, v120 row_half_mirror row_mask:0xf bank_mask:0xf
	s_nop 1
	v_mov_b32_dpp v124, v124 quad_perm:[3,2,1,0] row_mask:0xf bank_mask:0xf
	v_mov_b32_dpp v125, v121 row_half_mirror row_mask:0xf bank_mask:0xf
	s_nop 1
	v_mov_b32_dpp v125, v125 quad_perm:[3,2,1,0] row_mask:0xf bank_mask:0xf
	s_waitcnt lgkmcnt(0)
	v_pk_add_f32 v[122:123], v[122:123], v[126:127]
	s_nop 1
	v_mov_b32_dpp v126, v122 row_half_mirror row_mask:0xf bank_mask:0xf
	s_nop 1
	v_mov_b32_dpp v126, v126 quad_perm:[3,2,1,0] row_mask:0xf bank_mask:0xf
	v_mov_b32_dpp v127, v123 row_half_mirror row_mask:0xf bank_mask:0xf
	s_nop 1
	v_mov_b32_dpp v127, v127 quad_perm:[3,2,1,0] row_mask:0xf bank_mask:0xf
	v_mov_b32_dpp v7, v5 quad_perm:[1,0,3,2] row_mask:0xf bank_mask:0xf
	s_waitcnt lgkmcnt(0)
	v_pk_add_f32 v[120:121], v[120:121], v[124:125]
	s_nop 1
	v_mov_b32_dpp v124, v120 quad_perm:[2,3,0,1] row_mask:0xf bank_mask:0xf
	s_nop 0
	v_mov_b32_dpp v125, v121 quad_perm:[2,3,0,1] row_mask:0xf bank_mask:0xf
	s_waitcnt lgkmcnt(0)
	v_pk_add_f32 v[126:127], v[122:123], v[126:127]
	s_nop 1
	v_mov_b32_dpp v130, v126 quad_perm:[2,3,0,1] row_mask:0xf bank_mask:0xf
	s_nop 0
	v_mov_b32_dpp v131, v127 quad_perm:[2,3,0,1] row_mask:0xf bank_mask:0xf
	v_mov_b32_dpp v96, v8 quad_perm:[1,0,3,2] row_mask:0xf bank_mask:0xf
	s_waitcnt lgkmcnt(0)
	v_pk_add_f32 v[120:121], v[120:121], v[124:125]
	v_mov_b32_dpp v97, v9 quad_perm:[1,0,3,2] row_mask:0xf bank_mask:0xf
	v_mov_b32_dpp v10, v98 quad_perm:[1,0,3,2] row_mask:0xf bank_mask:0xf
	s_waitcnt lgkmcnt(0)
	v_pk_add_f32 v[124:125], v[126:127], v[130:131]
	v_mov_b32_dpp v11, v99 quad_perm:[1,0,3,2] row_mask:0xf bank_mask:0xf
	v_mov_b32_dpp v102, v100 quad_perm:[1,0,3,2] row_mask:0xf bank_mask:0xf
	v_mov_b32_dpp v103, v101 quad_perm:[1,0,3,2] row_mask:0xf bank_mask:0xf
	v_mov_b32_dpp v14, v12 quad_perm:[1,0,3,2] row_mask:0xf bank_mask:0xf
	v_mov_b32_dpp v15, v13 quad_perm:[1,0,3,2] row_mask:0xf bank_mask:0xf
	v_mov_b32_dpp v122, v120 quad_perm:[1,0,3,2] row_mask:0xf bank_mask:0xf
	v_mov_b32_dpp v123, v121 quad_perm:[1,0,3,2] row_mask:0xf bank_mask:0xf
	v_mov_b32_dpp v126, v124 quad_perm:[1,0,3,2] row_mask:0xf bank_mask:0xf
	v_mov_b32_dpp v127, v125 quad_perm:[1,0,3,2] row_mask:0xf bank_mask:0xf
	s_and_saveexec_b64 s[6:7], s[48:49]
	s_cbranch_execz .LBB0_360
	v_pk_add_f32 v[0:1], v[0:1], v[2:3]
	v_pk_add_f32 v[2:3], v[4:5], v[6:7]
	ds_write_b128 v231, v[0:3] offset:33792
	s_waitcnt lgkmcnt(11)
	v_pk_add_f32 v[0:1], v[8:9], v[96:97]
	s_waitcnt lgkmcnt(9)
	v_pk_add_f32 v[2:3], v[98:99], v[10:11]
	ds_write_b128 v231, v[0:3] offset:33824
	s_waitcnt lgkmcnt(8)
	v_pk_add_f32 v[0:1], v[100:101], v[102:103]
	s_waitcnt lgkmcnt(6)
	v_pk_add_f32 v[2:3], v[12:13], v[14:15]
	ds_write_b128 v231, v[0:3] offset:33856
	s_waitcnt lgkmcnt(5)
	v_pk_add_f32 v[0:1], v[120:121], v[122:123]
	s_waitcnt lgkmcnt(3)
	v_pk_add_f32 v[2:3], v[124:125], v[126:127]
	ds_write_b128 v231, v[0:3] offset:33888
.LBB0_360:
	s_or_b64 exec, exec, s[6:7]
	ds_read_b128 v[0:3], v229 offset:16896
	s_waitcnt lgkmcnt(11)
	ds_read_b128 v[96:99], v229 offset:16928
	s_waitcnt lgkmcnt(8)
	ds_read_b128 v[100:103], v229 offset:16960
	s_waitcnt lgkmcnt(5)
	ds_read_b128 v[120:123], v229 offset:16992
	s_nop 15
	s_nop 15
	s_waitcnt lgkmcnt(3)
	v_mfma_f32_32x32x16_bf16 v[0:15], v[0:3], v[76:79], 0
	s_waitcnt lgkmcnt(2)
	v_mfma_f32_32x32x16_bf16 v[0:15], v[96:99], v[72:75], v[0:15]
	s_waitcnt lgkmcnt(1)
	v_mfma_f32_32x32x16_bf16 v[0:15], v[100:103], v[68:71], v[0:15]
	s_waitcnt lgkmcnt(0)
	v_mfma_f32_32x32x16_bf16 v[0:15], v[120:123], v[64:67], v[0:15]
	s_nop 15
	s_nop 15
	ds_read_b128 v[64:67], v229 offset:17024
	ds_read_b128 v[68:71], v229 offset:17056
	ds_read_b128 v[72:75], v229 offset:17088
	ds_read_b128 v[76:79], v229 offset:17120
	s_nop 15
	s_nop 15
	s_waitcnt lgkmcnt(3)
	v_mfma_f32_32x32x16_bf16 v[0:15], v[64:67], v[60:63], v[0:15]
	s_waitcnt lgkmcnt(2)
	v_mfma_f32_32x32x16_bf16 v[0:15], v[68:71], v[56:59], v[0:15]
	s_waitcnt lgkmcnt(1)
	v_mfma_f32_32x32x16_bf16 v[0:15], v[72:75], v[52:55], v[0:15]
	s_waitcnt lgkmcnt(0)
	v_mfma_f32_32x32x16_bf16 v[0:15], v[76:79], v[48:51], v[0:15]
	s_nop 15
	s_nop 15
	ds_read_b128 v[48:51], v229 offset:17152
	ds_read_b128 v[52:55], v229 offset:17184
	ds_read_b128 v[56:59], v229 offset:17216
	ds_read_b128 v[60:63], v229 offset:17248
	s_nop 15
	s_nop 15
	s_waitcnt lgkmcnt(3)
	v_mfma_f32_32x32x16_bf16 v[0:15], v[48:51], v[44:47], v[0:15]
	s_waitcnt lgkmcnt(2)
	v_mfma_f32_32x32x16_bf16 v[0:15], v[52:55], v[40:43], v[0:15]
	s_waitcnt lgkmcnt(1)
	v_mfma_f32_32x32x16_bf16 v[0:15], v[56:59], v[36:39], v[0:15]
	s_waitcnt lgkmcnt(0)
	v_mfma_f32_32x32x16_bf16 v[0:15], v[60:63], v[32:35], v[0:15]
	s_nop 15
	s_nop 15
	ds_read_b128 v[32:35], v229 offset:17280
	ds_read_b128 v[36:39], v229 offset:17312
	ds_read_b128 v[40:43], v229 offset:17344
	ds_read_b128 v[44:47], v229 offset:17376
	s_nop 15
	s_nop 15
	s_waitcnt lgkmcnt(3)
	v_mfma_f32_32x32x16_bf16 v[0:15], v[32:35], v[28:31], v[0:15]
	s_waitcnt lgkmcnt(2)
	v_mfma_f32_32x32x16_bf16 v[0:15], v[36:39], v[24:27], v[0:15]
	s_waitcnt lgkmcnt(1)
	v_mfma_f32_32x32x16_bf16 v[0:15], v[40:43], v[20:23], v[0:15]
	s_waitcnt lgkmcnt(0)
	v_mfma_f32_32x32x16_bf16 v[0:15], v[44:47], v[16:19], v[0:15]
	s_nop 15
	s_nop 15
	s_nop 11
	v_add_f32_e32 v0, v129, v0
	v_add_f32_e32 v1, v129, v1
	v_mul_f32_e32 v0, 0xbfb8aa3b, v0
	v_mul_f32_e32 v1, 0xbfb8aa3b, v1
	v_exp_f32_e32 v0, v0
	v_exp_f32_e32 v1, v1
	ds_read_u16 v16, v228
	ds_read_u16 v17, v230 offset:17424
	ds_read_u16 v20, v230 offset:17952
	ds_read_u16 v21, v230 offset:18480
	ds_read_u16 v27, v230 offset:21120
	ds_read_u16 v28, v230 offset:21648
	ds_read_u16 v30, v230 offset:22176
	ds_read_u16 v29, v230 offset:22704
	ds_read_u16 v33, v230 offset:25344
	s_waitcnt lgkmcnt(7)
	v_lshlrev_b32_e32 v17, 16, v17
	v_add_f32_e32 v0, 1.0, v0
	v_add_f32_e32 v1, 1.0, v1
	v_rcp_f32_e32 v0, v0
	v_rcp_f32_e32 v1, v1
	v_lshlrev_b32_e32 v16, 16, v16
	v_add_f32_e32 v2, v129, v2
	v_mul_f32_e32 v2, 0xbfb8aa3b, v2
	v_pk_mul_f32 v[16:17], v[0:1], v[16:17]
	s_waitcnt lgkmcnt(5)
	v_lshlrev_b32_e32 v21, 16, v21
	v_pk_mul_f32 v[0:1], v[16:17], v[16:17]
	ds_bpermute_b32 v0, v185, v0
	ds_bpermute_b32 v1, v185, v1
	v_lshlrev_b32_e32 v20, 16, v20
	v_add_f32_e32 v6, v129, v6
	v_mul_f32_e32 v6, 0xbfb8aa3b, v6
	s_waitcnt lgkmcnt(3)
	v_lshlrev_b32_e32 v29, 16, v29
	s_waitcnt lgkmcnt(0)
	v_pk_fma_f32 v[0:1], v[16:17], v[16:17], v[0:1]
	s_nop 1
	v_mov_b32_dpp v18, v0 row_ror:8 row_mask:0xf bank_mask:0xf
	s_nop 0
	v_mov_b32_dpp v19, v1 row_ror:8 row_mask:0xf bank_mask:0xf
	ds_read_u16 v44, v230 offset:31152
	ds_read_u16 v34, v230 offset:25872
	ds_read_u16 v40, v230 offset:26400
	ds_read_u16 v41, v230 offset:26928
	ds_read_u16 v45, v230 offset:29568
	ds_read_u16 v46, v230 offset:30096
	ds_read_u16 v47, v230 offset:30624
	v_add_f32_e32 v12, v129, v12
	v_mul_f32_e32 v12, 0xbfb8aa3b, v12
	s_waitcnt lgkmcnt(0)
	v_pk_add_f32 v[0:1], v[0:1], v[18:19]
	v_exp_f32_e32 v18, v2
	v_add_f32_e32 v2, v129, v3
	v_mul_f32_e32 v2, 0xbfb8aa3b, v2
	v_exp_f32_e32 v3, v2
	s_nop 0
	v_mov_b32_dpp v2, v0 row_half_mirror row_mask:0xf bank_mask:0xf
	s_nop 1
	v_mov_b32_dpp v2, v2 quad_perm:[3,2,1,0] row_mask:0xf bank_mask:0xf
	v_add_f32_e32 v18, 1.0, v18
	v_rcp_f32_e32 v18, v18
	v_add_f32_e32 v3, 1.0, v3
	v_rcp_f32_e32 v19, v3
	s_nop 0
	v_mov_b32_dpp v3, v1 row_half_mirror row_mask:0xf bank_mask:0xf
	s_nop 1
	v_mov_b32_dpp v3, v3 quad_perm:[3,2,1,0] row_mask:0xf bank_mask:0xf
	v_add_f32_e32 v14, v129, v14
	v_mul_f32_e32 v14, 0xbfb8aa3b, v14
	v_pk_mul_f32 v[18:19], v[18:19], v[20:21]
	s_waitcnt lgkmcnt(0)
	v_pk_add_f32 v[0:1], v[0:1], v[2:3]
	s_nop 1
	v_mov_b32_dpp v2, v0 quad_perm:[2,3,0,1] row_mask:0xf bank_mask:0xf
	s_nop 0
	v_mov_b32_dpp v3, v1 quad_perm:[2,3,0,1] row_mask:0xf bank_mask:0xf
	v_pk_mul_f32 v[20:21], v[18:19], v[18:19]
	ds_bpermute_b32 v20, v185, v20
	ds_bpermute_b32 v21, v185, v21
	s_waitcnt lgkmcnt(0)
	v_pk_add_f32 v[24:25], v[0:1], v[2:3]
	v_add_f32_e32 v2, v129, v4
	v_mul_f32_e32 v2, 0xbfb8aa3b, v2
	v_exp_f32_e32 v3, v2
	v_add_f32_e32 v2, v129, v5
	v_mul_f32_e32 v2, 0xbfb8aa3b, v2
	v_exp_f32_e32 v5, v2
	s_waitcnt lgkmcnt(0)
	v_pk_fma_f32 v[20:21], v[18:19], v[18:19], v[20:21]
	s_nop 1
	v_mov_b32_dpp v22, v20 row_ror:8 row_mask:0xf bank_mask:0xf
	s_nop 0
	v_mov_b32_dpp v23, v21 row_ror:8 row_mask:0xf bank_mask:0xf
	v_add_f32_e32 v3, 1.0, v3
	v_rcp_f32_e32 v4, v3
	v_add_f32_e32 v3, 1.0, v5
	v_rcp_f32_e32 v5, v3
	s_waitcnt lgkmcnt(0)
	v_pk_add_f32 v[0:1], v[20:21], v[22:23]
	v_lshlrev_b32_e32 v21, 16, v28
	v_lshlrev_b32_e32 v20, 16, v27
	v_pk_mul_f32 v[20:21], v[4:5], v[20:21]
	v_exp_f32_e32 v22, v6
	v_add_f32_e32 v6, v129, v7
	v_pk_mul_f32 v[4:5], v[20:21], v[20:21]
	v_mul_f32_e32 v6, 0xbfb8aa3b, v6
	v_mov_b32_dpp v2, v0 row_half_mirror row_mask:0xf bank_mask:0xf
	s_nop 1
	v_mov_b32_dpp v2, v2 quad_perm:[3,2,1,0] row_mask:0xf bank_mask:0xf
	v_mov_b32_dpp v3, v1 row_half_mirror row_mask:0xf bank_mask:0xf
	s_nop 1
	v_mov_b32_dpp v3, v3 quad_perm:[3,2,1,0] row_mask:0xf bank_mask:0xf
	ds_bpermute_b32 v4, v185, v4
	ds_bpermute_b32 v5, v185, v5
	v_exp_f32_e32 v7, v6
	v_add_f32_e32 v22, 1.0, v22
	s_waitcnt lgkmcnt(0)
	v_pk_add_f32 v[0:1], v[0:1], v[2:3]
	v_rcp_f32_e32 v22, v22
	v_add_f32_e32 v7, 1.0, v7
	s_waitcnt lgkmcnt(0)
	v_pk_fma_f32 v[4:5], v[20:21], v[20:21], v[4:5]
	v_rcp_f32_e32 v23, v7
	v_mov_b32_dpp v2, v0 quad_perm:[2,3,0,1] row_mask:0xf bank_mask:0xf
	v_mov_b32_dpp v3, v1 quad_perm:[2,3,0,1] row_mask:0xf bank_mask:0xf
	v_mov_b32_dpp v6, v4 row_ror:8 row_mask:0xf bank_mask:0xf
	v_mov_b32_dpp v7, v5 row_ror:8 row_mask:0xf bank_mask:0xf
	v_lshlrev_b32_e32 v28, 16, v30
	v_pk_mul_f32 v[22:23], v[22:23], v[28:29]
	v_mov_b32_dpp v26, v24 quad_perm:[1,0,3,2] row_mask:0xf bank_mask:0xf
	v_pk_mul_f32 v[28:29], v[22:23], v[22:23]
	ds_bpermute_b32 v30, v185, v28
	ds_bpermute_b32 v31, v185, v29
	s_waitcnt lgkmcnt(0)
	v_pk_add_f32 v[28:29], v[0:1], v[2:3]
	s_waitcnt lgkmcnt(0)
	v_pk_add_f32 v[0:1], v[4:5], v[6:7]
	s_nop 1
	v_mov_b32_dpp v2, v0 row_half_mirror row_mask:0xf bank_mask:0xf
	s_nop 1
	v_mov_b32_dpp v2, v2 quad_perm:[3,2,1,0] row_mask:0xf bank_mask:0xf
	v_mov_b32_dpp v3, v1 row_half_mirror row_mask:0xf bank_mask:0xf
	s_nop 1
	v_mov_b32_dpp v3, v3 quad_perm:[3,2,1,0] row_mask:0xf bank_mask:0xf
	s_waitcnt lgkmcnt(0)
	v_pk_fma_f32 v[4:5], v[22:23], v[22:23], v[30:31]
	s_nop 1
	v_mov_b32_dpp v6, v4 row_ror:8 row_mask:0xf bank_mask:0xf
	s_nop 0
	v_mov_b32_dpp v7, v5 row_ror:8 row_mask:0xf bank_mask:0xf
	v_mov_b32_dpp v27, v25 quad_perm:[1,0,3,2] row_mask:0xf bank_mask:0xf
	s_waitcnt lgkmcnt(0)
	v_pk_add_f32 v[2:3], v[0:1], v[2:3]
	v_add_f32_e32 v0, v129, v8
	v_add_f32_e32 v1, v129, v9
	v_mul_f32_e32 v0, 0xbfb8aa3b, v0
	v_mul_f32_e32 v1, 0xbfb8aa3b, v1
	v_exp_f32_e32 v0, v0
	v_exp_f32_e32 v1, v1
	v_lshlrev_b32_e32 v9, 16, v34
	v_lshlrev_b32_e32 v8, 16, v33
	v_add_f32_e32 v0, 1.0, v0
	v_add_f32_e32 v1, 1.0, v1
	v_rcp_f32_e32 v0, v0
	v_rcp_f32_e32 v1, v1
	v_mov_b32_dpp v32, v2 quad_perm:[2,3,0,1] row_mask:0xf bank_mask:0xf
	v_mov_b32_dpp v33, v3 quad_perm:[2,3,0,1] row_mask:0xf bank_mask:0xf
	s_waitcnt lgkmcnt(0)
	v_pk_add_f32 v[4:5], v[4:5], v[6:7]
	v_pk_mul_f32 v[0:1], v[0:1], v[8:9]
	s_nop 0
	v_mov_b32_dpp v6, v4 row_half_mirror row_mask:0xf bank_mask:0xf
	s_nop 1
	v_mov_b32_dpp v6, v6 quad_perm:[3,2,1,0] row_mask:0xf bank_mask:0xf
	v_pk_mul_f32 v[8:9], v[0:1], v[0:1]
	ds_bpermute_b32 v8, v185, v8
	ds_bpermute_b32 v9, v185, v9
	v_mov_b32_dpp v7, v5 row_half_mirror row_mask:0xf bank_mask:0xf
	s_nop 1
	v_mov_b32_dpp v7, v7 quad_perm:[3,2,1,0] row_mask:0xf bank_mask:0xf
	v_mov_b32_dpp v30, v28 quad_perm:[1,0,3,2] row_mask:0xf bank_mask:0xf
	v_mov_b32_dpp v31, v29 quad_perm:[1,0,3,2] row_mask:0xf bank_mask:0xf
	s_waitcnt lgkmcnt(0)
	v_pk_fma_f32 v[36:37], v[0:1], v[0:1], v[8:9]
	v_pk_add_f32 v[8:9], v[2:3], v[32:33]
	v_add_f32_e32 v2, v129, v10
	v_add_f32_e32 v3, v129, v11
	v_mul_f32_e32 v2, 0xbfb8aa3b, v2
	v_mul_f32_e32 v3, 0xbfb8aa3b, v3
	v_exp_f32_e32 v2, v2
	v_exp_f32_e32 v3, v3
	s_waitcnt lgkmcnt(0)
	v_pk_add_f32 v[4:5], v[4:5], v[6:7]
	s_nop 1
	v_mov_b32_dpp v6, v4 quad_perm:[2,3,0,1] row_mask:0xf bank_mask:0xf
	v_add_f32_e32 v2, 1.0, v2
	v_add_f32_e32 v3, 1.0, v3
	v_mov_b32_dpp v7, v5 quad_perm:[2,3,0,1] row_mask:0xf bank_mask:0xf
	v_mov_b32_dpp v38, v36 row_ror:8 row_mask:0xf bank_mask:0xf
	v_mov_b32_dpp v39, v37 row_ror:8 row_mask:0xf bank_mask:0xf
	v_rcp_f32_e32 v2, v2
	v_rcp_f32_e32 v3, v3
	v_lshlrev_b32_e32 v11, 16, v41
	v_lshlrev_b32_e32 v10, 16, v40
	s_waitcnt lgkmcnt(0)
	v_pk_add_f32 v[34:35], v[4:5], v[6:7]
	v_pk_mul_f32 v[2:3], v[2:3], v[10:11]
	s_waitcnt lgkmcnt(0)
	v_pk_add_f32 v[4:5], v[36:37], v[38:39]
	v_pk_mul_f32 v[10:11], v[2:3], v[2:3]
	s_nop 0
	v_mov_b32_dpp v6, v4 row_half_mirror row_mask:0xf bank_mask:0xf
	s_nop 1
	v_mov_b32_dpp v6, v6 quad_perm:[3,2,1,0] row_mask:0xf bank_mask:0xf
	v_mov_b32_dpp v7, v5 row_half_mirror row_mask:0xf bank_mask:0xf
	s_nop 1
	v_mov_b32_dpp v7, v7 quad_perm:[3,2,1,0] row_mask:0xf bank_mask:0xf
	ds_bpermute_b32 v36, v185, v10
	ds_bpermute_b32 v37, v185, v11
	v_mov_b32_dpp v32, v8 quad_perm:[1,0,3,2] row_mask:0xf bank_mask:0xf
	v_mov_b32_dpp v33, v9 quad_perm:[1,0,3,2] row_mask:0xf bank_mask:0xf
	s_waitcnt lgkmcnt(0)
	v_pk_add_f32 v[4:5], v[4:5], v[6:7]
	s_nop 1
	v_mov_b32_dpp v6, v4 quad_perm:[2,3,0,1] row_mask:0xf bank_mask:0xf
	s_waitcnt lgkmcnt(0)
	v_pk_fma_f32 v[40:41], v[2:3], v[2:3], v[36:37]
	v_mov_b32_dpp v7, v5 quad_perm:[2,3,0,1] row_mask:0xf bank_mask:0xf
	s_nop 0
	v_mov_b32_dpp v42, v40 row_ror:8 row_mask:0xf bank_mask:0xf
	v_mov_b32_dpp v43, v41 row_ror:8 row_mask:0xf bank_mask:0xf
	v_mov_b32_dpp v10, v34 quad_perm:[1,0,3,2] row_mask:0xf bank_mask:0xf
	v_mov_b32_dpp v11, v35 quad_perm:[1,0,3,2] row_mask:0xf bank_mask:0xf
	s_waitcnt lgkmcnt(0)
	v_pk_add_f32 v[36:37], v[4:5], v[6:7]
	s_nop 1
	v_mov_b32_dpp v38, v36 quad_perm:[1,0,3,2] row_mask:0xf bank_mask:0xf
	s_waitcnt lgkmcnt(0)
	v_pk_add_f32 v[4:5], v[40:41], v[42:43]
	v_exp_f32_e32 v40, v12
	v_add_f32_e32 v12, v129, v13
	v_mov_b32_dpp v6, v4 row_half_mirror row_mask:0xf bank_mask:0xf
	s_nop 1
	v_mov_b32_dpp v6, v6 quad_perm:[3,2,1,0] row_mask:0xf bank_mask:0xf
	v_mov_b32_dpp v7, v5 row_half_mirror row_mask:0xf bank_mask:0xf
	s_nop 1
	v_mov_b32_dpp v7, v7 quad_perm:[3,2,1,0] row_mask:0xf bank_mask:0xf
	v_mul_f32_e32 v12, 0xbfb8aa3b, v12
	v_exp_f32_e32 v41, v12
	v_mov_b32_dpp v39, v37 quad_perm:[1,0,3,2] row_mask:0xf bank_mask:0xf
	s_waitcnt lgkmcnt(0)
	v_pk_add_f32 v[12:13], v[4:5], v[6:7]
	v_add_f32_e32 v4, 1.0, v40
	v_add_f32_e32 v5, 1.0, v41
	v_rcp_f32_e32 v4, v4
	v_rcp_f32_e32 v5, v5
	v_exp_f32_e32 v41, v14
	v_add_f32_e32 v14, v129, v15
	v_mul_f32_e32 v14, 0xbfb8aa3b, v14
	v_lshlrev_b32_e32 v7, 16, v46
	v_lshlrev_b32_e32 v6, 16, v45
	v_exp_f32_e32 v15, v14
	v_pk_mul_f32 v[4:5], v[4:5], v[6:7]
	v_mov_b32_dpp v40, v12 quad_perm:[2,3,0,1] row_mask:0xf bank_mask:0xf
	v_pk_mul_f32 v[6:7], v[4:5], v[4:5]
	ds_bpermute_b32 v14, v185, v6
	v_add_f32_e32 v6, 1.0, v41
	v_rcp_f32_e32 v42, v6
	v_add_f32_e32 v6, 1.0, v15
	v_rcp_f32_e32 v43, v6
	ds_bpermute_b32 v15, v185, v7
	v_lshlrev_b32_e32 v7, 16, v44
	v_lshlrev_b32_e32 v6, 16, v47
	v_pk_mul_f32 v[6:7], v[42:43], v[6:7]
	v_mov_b32_dpp v41, v13 quad_perm:[2,3,0,1] row_mask:0xf bank_mask:0xf
	v_pk_mul_f32 v[42:43], v[6:7], v[6:7]
	ds_bpermute_b32 v42, v185, v42
	ds_bpermute_b32 v43, v185, v43
	s_waitcnt lgkmcnt(0)
	v_pk_fma_f32 v[14:15], v[4:5], v[4:5], v[14:15]
	s_nop 1
	v_mov_b32_dpp v44, v14 row_ror:8 row_mask:0xf bank_mask:0xf
	s_nop 0
	v_mov_b32_dpp v45, v15 row_ror:8 row_mask:0xf bank_mask:0xf
	s_waitcnt lgkmcnt(0)
	v_pk_add_f32 v[12:13], v[12:13], v[40:41]
	s_waitcnt lgkmcnt(0)
	v_pk_fma_f32 v[42:43], v[6:7], v[6:7], v[42:43]
	s_nop 1
	v_mov_b32_dpp v46, v42 row_ror:8 row_mask:0xf bank_mask:0xf
	s_nop 0
	v_mov_b32_dpp v47, v43 row_ror:8 row_mask:0xf bank_mask:0xf
	s_waitcnt lgkmcnt(0)
	v_pk_add_f32 v[40:41], v[14:15], v[44:45]
	s_nop 1
	v_mov_b32_dpp v44, v40 row_half_mirror row_mask:0xf bank_mask:0xf
	s_nop 1
	v_mov_b32_dpp v44, v44 quad_perm:[3,2,1,0] row_mask:0xf bank_mask:0xf
	v_mov_b32_dpp v45, v41 row_half_mirror row_mask:0xf bank_mask:0xf
	s_nop 1
	v_mov_b32_dpp v45, v45 quad_perm:[3,2,1,0] row_mask:0xf bank_mask:0xf
	v_mov_b32_dpp v14, v12 quad_perm:[1,0,3,2] row_mask:0xf bank_mask:0xf
	s_waitcnt lgkmcnt(0)
	v_pk_add_f32 v[42:43], v[42:43], v[46:47]
	s_nop 1
	v_mov_b32_dpp v46, v42 row_half_mirror row_mask:0xf bank_mask:0xf
	s_nop 1
	v_mov_b32_dpp v46, v46 quad_perm:[3,2,1,0] row_mask:0xf bank_mask:0xf
	v_mov_b32_dpp v47, v43 row_half_mirror row_mask:0xf bank_mask:0xf
	s_nop 1
	v_mov_b32_dpp v47, v47 quad_perm:[3,2,1,0] row_mask:0xf bank_mask:0xf
	s_waitcnt lgkmcnt(0)
	v_pk_add_f32 v[40:41], v[40:41], v[44:45]
	s_nop 1
	v_mov_b32_dpp v44, v40 quad_perm:[2,3,0,1] row_mask:0xf bank_mask:0xf
	s_nop 0
	v_mov_b32_dpp v45, v41 quad_perm:[2,3,0,1] row_mask:0xf bank_mask:0xf
	v_mov_b32_dpp v15, v13 quad_perm:[1,0,3,2] row_mask:0xf bank_mask:0xf
	s_waitcnt lgkmcnt(0)
	v_pk_add_f32 v[46:47], v[42:43], v[46:47]
	s_nop 1
	v_mov_b32_dpp v48, v46 quad_perm:[2,3,0,1] row_mask:0xf bank_mask:0xf
	s_nop 0
	v_mov_b32_dpp v49, v47 quad_perm:[2,3,0,1] row_mask:0xf bank_mask:0xf
	s_waitcnt lgkmcnt(0)
	v_pk_add_f32 v[40:41], v[40:41], v[44:45]
	s_nop 1
	v_mov_b32_dpp v42, v40 quad_perm:[1,0,3,2] row_mask:0xf bank_mask:0xf
	s_nop 0
	v_mov_b32_dpp v43, v41 quad_perm:[1,0,3,2] row_mask:0xf bank_mask:0xf
	s_waitcnt lgkmcnt(0)
	v_pk_add_f32 v[44:45], v[46:47], v[48:49]
	s_nop 1
	v_mov_b32_dpp v46, v44 quad_perm:[1,0,3,2] row_mask:0xf bank_mask:0xf
	s_nop 0
	v_mov_b32_dpp v47, v45 quad_perm:[1,0,3,2] row_mask:0xf bank_mask:0xf
	s_and_saveexec_b64 s[6:7], s[48:49]
	s_cbranch_execz .LBB0_362
	v_pk_add_f32 v[8:9], v[8:9], v[32:33]
	v_pk_add_f32 v[10:11], v[34:35], v[10:11]
	ds_write_b128 v231, v[8:11] offset:33952
	v_pk_add_f32 v[8:9], v[36:37], v[38:39]
	v_pk_add_f32 v[10:11], v[12:13], v[14:15]
	v_pk_add_f32 v[24:25], v[24:25], v[26:27]
	v_pk_add_f32 v[26:27], v[28:29], v[30:31]
	ds_write_b128 v231, v[8:11] offset:33984
	s_waitcnt lgkmcnt(4)
	v_pk_add_f32 v[8:9], v[40:41], v[42:43]
	s_waitcnt lgkmcnt(2)
	v_pk_add_f32 v[10:11], v[44:45], v[46:47]
	ds_write_b128 v231, v[24:27] offset:33920
	ds_write_b128 v231, v[8:11] offset:34016
